# NA key staging: fp8->f32 direct (exact bf16 pack/unpack round trip dropped), 16-lane sum of squares via DPP adds instead of 4 ds_bpermute round trips
# speedup vs baseline: 1.0925x; 1.0069x over previous
.LBB0_601:
	v_cndmask_b32_e64 v184, v98, v184, s[72:73]
	v_mul_f32_e32 v98, 0xbe0293ee, v184
	v_fmamk_f32 v82, v82, 0x3e0293ee, v98
	v_fmamk_f32 v83, v83, 0x3e0293ee, v98
	v_fmamk_f32 v84, v84, 0x3e0293ee, v98
	v_fmamk_f32 v85, v85, 0x3e0293ee, v98
	v_fmamk_f32 v86, v86, 0x3e0293ee, v98
	v_fmamk_f32 v87, v87, 0x3e0293ee, v98
	v_fmamk_f32 v88, v88, 0x3e0293ee, v98
	v_fmamk_f32 v89, v89, 0x3e0293ee, v98
	v_fmamk_f32 v90, v90, 0x3e0293ee, v98
	v_fmamk_f32 v91, v91, 0x3e0293ee, v98
	v_fmamk_f32 v92, v92, 0x3e0293ee, v98
	v_fmamk_f32 v93, v93, 0x3e0293ee, v98
	v_fmamk_f32 v94, v94, 0x3e0293ee, v98
	v_fmamk_f32 v95, v95, 0x3e0293ee, v98
	v_fmamk_f32 v96, v96, 0x3e0293ee, v98
	v_fmamk_f32 v97, v97, 0x3e0293ee, v98
	v_fmamk_f32 v0, v0, 0x3e0293ee, v98
	v_fmamk_f32 v66, v66, 0x3e0293ee, v98
	v_fmamk_f32 v67, v67, 0x3e0293ee, v98
	v_fmamk_f32 v68, v68, 0x3e0293ee, v98
	v_fmamk_f32 v69, v69, 0x3e0293ee, v98
	v_fmamk_f32 v70, v70, 0x3e0293ee, v98
	v_fmamk_f32 v71, v71, 0x3e0293ee, v98
	v_fmamk_f32 v72, v72, 0x3e0293ee, v98
	v_fmamk_f32 v73, v73, 0x3e0293ee, v98
	v_fmamk_f32 v74, v74, 0x3e0293ee, v98
	v_fmamk_f32 v75, v75, 0x3e0293ee, v98
	v_fmamk_f32 v76, v76, 0x3e0293ee, v98
	v_fmamk_f32 v77, v77, 0x3e0293ee, v98
	v_fmamk_f32 v78, v78, 0x3e0293ee, v98
	v_fmamk_f32 v79, v79, 0x3e0293ee, v98
	v_fmac_f32_e32 v98, 0x3e0293ee, v80
	v_exp_f32_e32 v80, v82
	v_exp_f32_e32 v82, v83
	v_exp_f32_e32 v83, v84
	v_exp_f32_e32 v84, v85
	v_exp_f32_e32 v85, v86
	v_exp_f32_e32 v86, v87
	v_exp_f32_e32 v87, v88
	v_exp_f32_e32 v88, v89
	v_exp_f32_e32 v89, v90
	v_exp_f32_e32 v90, v91
	v_exp_f32_e32 v91, v92
	v_exp_f32_e32 v92, v93
	v_exp_f32_e32 v93, v94
	v_exp_f32_e32 v94, v95
	v_exp_f32_e32 v95, v96
	v_exp_f32_e32 v96, v97
	v_exp_f32_e32 v97, v0
	v_add_f32_e32 v0, 0, v80
	v_add_f32_e32 v0, v82, v0
	v_add_f32_e32 v0, v83, v0
	v_add_f32_e32 v0, v84, v0
	v_add_f32_e32 v0, v85, v0
	v_add_f32_e32 v0, v86, v0
	v_add_f32_e32 v0, v87, v0
	v_add_f32_e32 v0, v88, v0
	v_add_f32_e32 v0, v89, v0
	v_add_f32_e32 v0, v90, v0
	v_add_f32_e32 v0, v91, v0
	v_add_f32_e32 v0, v92, v0
	v_add_f32_e32 v0, v93, v0
	v_exp_f32_e32 v99, v66
	v_add_f32_e32 v0, v94, v0
	v_exp_f32_e32 v100, v67
	v_add_f32_e32 v0, v95, v0
	v_exp_f32_e32 v101, v68
	v_add_f32_e32 v0, v96, v0
	v_exp_f32_e32 v102, v69
	v_add_f32_e32 v0, v97, v0
	v_exp_f32_e32 v103, v70
	v_add_f32_e32 v0, v99, v0
	v_exp_f32_e32 v104, v71
	v_add_f32_e32 v0, v100, v0
	v_exp_f32_e32 v105, v72
	v_add_f32_e32 v0, v101, v0
	v_exp_f32_e32 v106, v73
	v_add_f32_e32 v0, v102, v0
	v_exp_f32_e32 v107, v74
	v_add_f32_e32 v0, v103, v0
	v_exp_f32_e32 v108, v75
	v_add_f32_e32 v0, v104, v0
	v_exp_f32_e32 v109, v76
	v_add_f32_e32 v0, v105, v0
	v_exp_f32_e32 v110, v77
	v_add_f32_e32 v0, v106, v0
	v_exp_f32_e32 v111, v78
	v_add_f32_e32 v0, v107, v0
	v_exp_f32_e32 v112, v79
	v_add_f32_e32 v0, v108, v0
	v_exp_f32_e32 v98, v98
	v_add_f32_e32 v0, v109, v0
	v_add_f32_e32 v0, v110, v0
	v_add_f32_e32 v0, v111, v0
	v_add_f32_e32 v0, v112, v0
	v_add_f32_e32 v0, v98, v0
	v_mov_b32_e32 v66, v0
	s_nop 1
	v_permlane32_swap_b32_e32 v0, v66
	v_add_f32_e32 v0, v0, v66
	v_fmac_f32_e32 v0, v200, v81
	v_cvt_pk_bf16_f32 v66, v80, v82
	v_cvt_pk_bf16_f32 v67, v83, v84
	v_cvt_pk_bf16_f32 v68, v85, v86
	v_cvt_pk_bf16_f32 v69, v87, v88
	v_cvt_pk_bf16_f32 v70, v89, v90
	v_cvt_pk_bf16_f32 v71, v91, v92
	v_cvt_pk_bf16_f32 v72, v93, v94
	v_cvt_pk_bf16_f32 v73, v95, v96
	v_cvt_pk_bf16_f32 v74, v97, v99
	v_cvt_pk_bf16_f32 v75, v100, v101
	v_cvt_pk_bf16_f32 v76, v102, v103
	v_cvt_pk_bf16_f32 v77, v104, v105
	v_cvt_pk_bf16_f32 v78, v106, v107
	v_cvt_pk_bf16_f32 v79, v108, v109
	v_cvt_pk_bf16_f32 v80, v110, v111
	v_cvt_pk_bf16_f32 v81, v112, v98
	s_nop 0
	v_permlane32_swap_b32_e32 v66, v68
	v_permlane32_swap_b32_e32 v67, v69
	v_permlane32_swap_b32_e32 v70, v72
	v_permlane32_swap_b32_e32 v71, v73
	v_permlane32_swap_b32_e32 v74, v76
	v_permlane32_swap_b32_e32 v75, v77
	v_permlane32_swap_b32_e32 v78, v80
	v_permlane32_swap_b32_e32 v79, v81
	v_add_u32_e32 v98, s1, v182
	ds_read_b64_tr_b16 v[82:83], v98 offset:0
	ds_read_b64_tr_b16 v[84:85], v98 offset:0x800
	ds_read_b64_tr_b16 v[86:87], v98 offset:0x1000
	ds_read_b64_tr_b16 v[88:89], v98 offset:0x1800
	ds_read_b64_tr_b16 v[90:91], v98 offset:0x2000
	ds_read_b64_tr_b16 v[92:93], v98 offset:0x2800
	ds_read_b64_tr_b16 v[94:95], v98 offset:0x3000
	ds_read_b64_tr_b16 v[96:97], v98 offset:0x3800
	s_waitcnt lgkmcnt(0)
	s_nop 0
	v_mfma_f32_32x32x16_bf16 v[50:65], v[66:69], v[82:85], v[50:65]
	ds_read_b64_tr_b16 v[82:83], v98 offset:0x200
	ds_read_b64_tr_b16 v[84:85], v98 offset:0xa00
	v_mfma_f32_32x32x16_bf16 v[50:65], v[70:73], v[86:89], v[50:65]
	ds_read_b64_tr_b16 v[86:87], v98 offset:0x1200
	ds_read_b64_tr_b16 v[88:89], v98 offset:0x1a00
	v_mfma_f32_32x32x16_bf16 v[50:65], v[74:77], v[90:93], v[50:65]
	ds_read_b64_tr_b16 v[90:91], v98 offset:0x2200
	ds_read_b64_tr_b16 v[92:93], v98 offset:0x2a00
	v_mfma_f32_32x32x16_bf16 v[50:65], v[78:81], v[94:97], v[50:65]
	ds_read_b64_tr_b16 v[94:95], v98 offset:0x3200
	ds_read_b64_tr_b16 v[96:97], v98 offset:0x3a00
	s_waitcnt lgkmcnt(0)
	v_mfma_f32_32x32x16_bf16 v[34:49], v[66:69], v[82:85], v[34:49]
	ds_read_b64_tr_b16 v[82:83], v98 offset:0x400
	ds_read_b64_tr_b16 v[84:85], v98 offset:0xc00
	v_mfma_f32_32x32x16_bf16 v[34:49], v[70:73], v[86:89], v[34:49]
	ds_read_b64_tr_b16 v[86:87], v98 offset:0x1400
	ds_read_b64_tr_b16 v[88:89], v98 offset:0x1c00
	v_mfma_f32_32x32x16_bf16 v[34:49], v[74:77], v[90:93], v[34:49]
	ds_read_b64_tr_b16 v[90:91], v98 offset:0x2400
	ds_read_b64_tr_b16 v[92:93], v98 offset:0x2c00
	v_mfma_f32_32x32x16_bf16 v[34:49], v[78:81], v[94:97], v[34:49]
	ds_read_b64_tr_b16 v[94:95], v98 offset:0x3400
	ds_read_b64_tr_b16 v[96:97], v98 offset:0x3c00
	s_waitcnt lgkmcnt(0)
	v_mfma_f32_32x32x16_bf16 v[18:33], v[66:69], v[82:85], v[18:33]
	ds_read_b64_tr_b16 v[82:83], v98 offset:0x600
	ds_read_b64_tr_b16 v[84:85], v98 offset:0xe00
	v_mfma_f32_32x32x16_bf16 v[18:33], v[70:73], v[86:89], v[18:33]
	ds_read_b64_tr_b16 v[86:87], v98 offset:0x1600
	ds_read_b64_tr_b16 v[88:89], v98 offset:0x1e00
	v_mfma_f32_32x32x16_bf16 v[18:33], v[74:77], v[90:93], v[18:33]
	ds_read_b64_tr_b16 v[90:91], v98 offset:0x2600
	ds_read_b64_tr_b16 v[92:93], v98 offset:0x2e00
	v_mfma_f32_32x32x16_bf16 v[18:33], v[78:81], v[94:97], v[18:33]
	ds_read_b64_tr_b16 v[94:95], v98 offset:0x3600
	ds_read_b64_tr_b16 v[96:97], v98 offset:0x3e00
	s_waitcnt lgkmcnt(0)
	v_mfma_f32_32x32x16_bf16 v[2:17], v[66:69], v[82:85], v[2:17]
	s_waitcnt vmcnt(3)
	v_cvt_f32_fp8_e32 v66, v164
	v_cvt_f32_fp8_sdwa v67, v164 src0_sel:BYTE_1
	s_waitcnt vmcnt(0)
	v_cvt_pk_bf16_f32 v66, v66, v67
	v_cvt_f32_fp8_sdwa v67, v164 src0_sel:BYTE_2
	v_cvt_f32_fp8_sdwa v68, v164 src0_sel:BYTE_3
	v_cvt_pk_bf16_f32 v67, v67, v68
	v_mfma_f32_32x32x16_bf16 v[2:17], v[70:73], v[86:89], v[2:17]
	v_cvt_f32_fp8_e32 v68, v165
	v_cvt_f32_fp8_sdwa v69, v165 src0_sel:BYTE_1
	v_cvt_pk_bf16_f32 v68, v68, v69
	v_cvt_f32_fp8_sdwa v69, v165 src0_sel:BYTE_2
	v_cvt_f32_fp8_sdwa v70, v165 src0_sel:BYTE_3
	v_cvt_pk_bf16_f32 v69, v69, v70
	s_waitcnt vmcnt(2)
	v_cvt_f32_fp8_e32 v70, v162
	v_mfma_f32_32x32x16_bf16 v[2:17], v[74:77], v[90:93], v[2:17]
	v_cvt_f32_fp8_sdwa v71, v162 src0_sel:BYTE_1
	v_cvt_pk_bf16_f32 v70, v70, v71
	v_cvt_f32_fp8_sdwa v71, v162 src0_sel:BYTE_2
	v_cvt_f32_fp8_sdwa v72, v162 src0_sel:BYTE_3
	v_cvt_pk_bf16_f32 v71, v71, v72
	v_cvt_f32_fp8_e32 v72, v163
	v_cvt_f32_fp8_sdwa v73, v163 src0_sel:BYTE_1
	v_cvt_pk_bf16_f32 v72, v72, v73
	v_cvt_f32_fp8_sdwa v73, v163 src0_sel:BYTE_2
	v_cvt_f32_fp8_sdwa v74, v163 src0_sel:BYTE_3
	v_cvt_pk_bf16_f32 v73, v73, v74
	s_waitcnt vmcnt(1)
	v_mfma_f32_32x32x16_bf16 v[2:17], v[78:81], v[94:97], v[2:17]
	s_waitcnt vmcnt(0)
	v_cvt_f32_fp8_e32 v82, v160
	v_cvt_f32_fp8_sdwa v74, v160 src0_sel:BYTE_1
	v_cvt_f32_fp8_sdwa v83, v160 src0_sel:BYTE_2
	v_cvt_f32_fp8_sdwa v75, v160 src0_sel:BYTE_3
	v_mul_f32_e32 v86, v74, v74
	v_mul_f32_e32 v87, v75, v75
	v_cvt_f32_fp8_e32 v84, v161
	v_cvt_f32_fp8_sdwa v76, v161 src0_sel:BYTE_1
	v_fmac_f32_e32 v86, v82, v82
	v_fmac_f32_e32 v87, v83, v83
	v_add_f32_e32 v86, v86, v87
	v_mul_f32_e32 v87, v76, v76
	v_cvt_f32_fp8_sdwa v85, v161 src0_sel:BYTE_2
	v_cvt_f32_fp8_sdwa v77, v161 src0_sel:BYTE_3
	v_fmac_f32_e32 v87, v84, v84
	v_add_f32_e32 v86, v86, v87
	v_mul_f32_e32 v87, v77, v77
	v_fmac_f32_e32 v87, v85, v85
	v_add_f32_e32 v86, v86, v87
	s_nop 1
	s_xor_b32 s1, s1, 0x4000
	s_add_i32 s1, s1, 0
	s_add_i32 s92, s92, 1
	s_addk_i32 s3, 0x4000
	v_add_f32_dpp v86, v86, v86 quad_perm:[1,0,3,2] row_mask:0xf bank_mask:0xf
	s_nop 1
	s_add_u32 s96, s96, 0x2000
	s_addc_u32 s97, s97, 0
	s_cmp_eq_u32 s96, 0x16000
	v_add_f32_dpp v86, v86, v86 quad_perm:[2,3,0,1] row_mask:0xf bank_mask:0xf
	s_nop 1
	v_add_f32_dpp v86, v86, v86 row_half_mirror row_mask:0xf bank_mask:0xf
	s_nop 1
	s_waitcnt lgkmcnt(0)
	v_add_f32_dpp v86, v86, v86 row_mirror row_mask:0xf bank_mask:0xf
	v_fmamk_f32 v86, v86, 0x3c000000, v167
	v_rsq_f32_e32 v86, v86
	s_nop 0
	v_mul_f32_e32 v82, v86, v82
	v_mul_f32_e32 v74, v86, v74
	v_mul_f32_e32 v82, v150, v82
	v_mul_f32_e32 v74, v151, v74
	v_cvt_pk_bf16_f32 v74, v82, v74
	v_mul_f32_e32 v82, v86, v83
	v_mul_f32_e32 v75, v86, v75
	v_mul_f32_e32 v82, v152, v82
	v_mul_f32_e32 v75, v153, v75
	v_cvt_pk_bf16_f32 v75, v82, v75
	v_mul_f32_e32 v82, v86, v84
	v_mul_f32_e32 v76, v86, v76
	v_mul_f32_e32 v82, v146, v82
	v_mul_f32_e32 v76, v147, v76
	v_cvt_pk_bf16_f32 v76, v82, v76
	v_mul_f32_e32 v82, v86, v85
	v_mul_f32_e32 v77, v86, v77
	v_mul_f32_e32 v82, v148, v82
	v_mul_f32_e32 v77, v149, v77
	v_cvt_pk_bf16_f32 v77, v82, v77
	v_cvt_f32_fp8_e32 v82, v158
	v_cvt_f32_fp8_sdwa v78, v158 src0_sel:BYTE_1
	v_cvt_f32_fp8_sdwa v83, v158 src0_sel:BYTE_2
	v_cvt_f32_fp8_sdwa v79, v158 src0_sel:BYTE_3
	v_mul_f32_e32 v86, v78, v78
	v_mul_f32_e32 v87, v79, v79
	v_cvt_f32_fp8_e32 v84, v159
	v_cvt_f32_fp8_sdwa v80, v159 src0_sel:BYTE_1
	v_fmac_f32_e32 v86, v82, v82
	v_fmac_f32_e32 v87, v83, v83
	v_add_f32_e32 v86, v86, v87
	v_mul_f32_e32 v87, v80, v80
	v_cvt_f32_fp8_sdwa v85, v159 src0_sel:BYTE_2
	v_cvt_f32_fp8_sdwa v81, v159 src0_sel:BYTE_3
	v_fmac_f32_e32 v87, v84, v84
	v_add_f32_e32 v86, v86, v87
	v_mul_f32_e32 v87, v81, v81
	v_fmac_f32_e32 v87, v85, v85
	v_add_f32_e32 v86, v86, v87
	s_nop 1
	v_add_f32_dpp v86, v86, v86 quad_perm:[1,0,3,2] row_mask:0xf bank_mask:0xf
	s_nop 1
	v_add_f32_dpp v86, v86, v86 quad_perm:[2,3,0,1] row_mask:0xf bank_mask:0xf
	s_nop 1
	v_add_f32_dpp v86, v86, v86 row_half_mirror row_mask:0xf bank_mask:0xf
	s_nop 1
	s_waitcnt lgkmcnt(0)
	v_add_f32_dpp v86, v86, v86 row_mirror row_mask:0xf bank_mask:0xf
	v_fmamk_f32 v86, v86, 0x3c000000, v167
	v_rsq_f32_e32 v86, v86
	s_nop 0
	v_mul_f32_e32 v82, v86, v82
	v_mul_f32_e32 v78, v86, v78
	v_mul_f32_e32 v82, v150, v82
	v_mul_f32_e32 v78, v151, v78
	v_cvt_pk_bf16_f32 v78, v82, v78
	v_mul_f32_e32 v82, v86, v83
	v_mul_f32_e32 v79, v86, v79
	v_mul_f32_e32 v82, v152, v82
	v_mul_f32_e32 v79, v153, v79
	v_cvt_pk_bf16_f32 v79, v82, v79
	v_mul_f32_e32 v82, v86, v84
	v_mul_f32_e32 v80, v86, v80
	v_mul_f32_e32 v82, v146, v82
	v_mul_f32_e32 v80, v147, v80
	v_cvt_pk_bf16_f32 v80, v82, v80
	v_mul_f32_e32 v82, v86, v85
	v_mul_f32_e32 v81, v86, v81
	v_mul_f32_e32 v82, v148, v82
	v_mul_f32_e32 v81, v149, v81
	v_cvt_pk_bf16_f32 v81, v82, v81
	v_add_u32_e32 v82, s1, v180
	ds_write_b128 v82, v[66:69]
	v_add_u32_e32 v66, s1, v181
	ds_write_b128 v66, v[70:73]
	v_add_u32_e32 v66, s1, v196
	ds_write_b128 v66, v[74:77] offset:32768
	v_add_u32_e32 v66, s1, v198
	ds_write_b128 v66, v[78:81] offset:32768
	s_waitcnt lgkmcnt(0)
	s_barrier
	s_cbranch_scc1 .LBB0_603
	v_mov_b32_e32 v200, v0
	s_branch .LBB0_469
.Lna_skip:
	s_waitcnt vmcnt(3)
	v_cvt_f32_fp8_e32 v66, v164
	v_cvt_f32_fp8_sdwa v67, v164 src0_sel:BYTE_1
	s_waitcnt vmcnt(0)
	v_cvt_pk_bf16_f32 v66, v66, v67
	v_cvt_f32_fp8_sdwa v67, v164 src0_sel:BYTE_2
	v_cvt_f32_fp8_sdwa v68, v164 src0_sel:BYTE_3
	v_cvt_pk_bf16_f32 v67, v67, v68
	v_cvt_f32_fp8_e32 v68, v165
	v_cvt_f32_fp8_sdwa v69, v165 src0_sel:BYTE_1
	v_cvt_pk_bf16_f32 v68, v68, v69
	v_cvt_f32_fp8_sdwa v69, v165 src0_sel:BYTE_2
	v_cvt_f32_fp8_sdwa v70, v165 src0_sel:BYTE_3
	v_cvt_pk_bf16_f32 v69, v69, v70
	s_waitcnt vmcnt(2)
	v_cvt_f32_fp8_e32 v70, v162
	v_cvt_f32_fp8_sdwa v71, v162 src0_sel:BYTE_1
	v_cvt_pk_bf16_f32 v70, v70, v71
	v_cvt_f32_fp8_sdwa v71, v162 src0_sel:BYTE_2
	v_cvt_f32_fp8_sdwa v72, v162 src0_sel:BYTE_3
	v_cvt_pk_bf16_f32 v71, v71, v72
	v_cvt_f32_fp8_e32 v72, v163
	v_cvt_f32_fp8_sdwa v73, v163 src0_sel:BYTE_1
	v_cvt_pk_bf16_f32 v72, v72, v73
	v_cvt_f32_fp8_sdwa v73, v163 src0_sel:BYTE_2
	v_cvt_f32_fp8_sdwa v74, v163 src0_sel:BYTE_3
	v_cvt_pk_bf16_f32 v73, v73, v74
	s_waitcnt vmcnt(1)
	s_waitcnt vmcnt(0)
	v_cvt_f32_fp8_e32 v82, v160
	v_cvt_f32_fp8_sdwa v74, v160 src0_sel:BYTE_1
	v_cvt_f32_fp8_sdwa v83, v160 src0_sel:BYTE_2
	v_cvt_f32_fp8_sdwa v75, v160 src0_sel:BYTE_3
	v_mul_f32_e32 v86, v74, v74
	v_mul_f32_e32 v87, v75, v75
	v_cvt_f32_fp8_e32 v84, v161
	v_cvt_f32_fp8_sdwa v76, v161 src0_sel:BYTE_1
	v_fmac_f32_e32 v86, v82, v82
	v_fmac_f32_e32 v87, v83, v83
	v_add_f32_e32 v86, v86, v87
	v_mul_f32_e32 v87, v76, v76
	v_cvt_f32_fp8_sdwa v85, v161 src0_sel:BYTE_2
	v_cvt_f32_fp8_sdwa v77, v161 src0_sel:BYTE_3
	v_fmac_f32_e32 v87, v84, v84
	v_add_f32_e32 v86, v86, v87
	v_mul_f32_e32 v87, v77, v77
	v_fmac_f32_e32 v87, v85, v85
	v_add_f32_e32 v86, v86, v87
	s_nop 1
	s_xor_b32 s1, s1, 0x4000
	s_add_i32 s1, s1, 0
	s_add_i32 s92, s92, 1
	s_addk_i32 s3, 0x4000
	v_add_f32_dpp v86, v86, v86 quad_perm:[1,0,3,2] row_mask:0xf bank_mask:0xf
	s_nop 1
	s_add_u32 s96, s96, 0x2000
	s_addc_u32 s97, s97, 0
	s_cmp_eq_u32 s96, 0x16000
	v_add_f32_dpp v86, v86, v86 quad_perm:[2,3,0,1] row_mask:0xf bank_mask:0xf
	s_nop 1
	v_add_f32_dpp v86, v86, v86 row_half_mirror row_mask:0xf bank_mask:0xf
	s_nop 1
	s_waitcnt lgkmcnt(0)
	v_add_f32_dpp v86, v86, v86 row_mirror row_mask:0xf bank_mask:0xf
	v_fmamk_f32 v86, v86, 0x3c000000, v167
	v_rsq_f32_e32 v86, v86
	s_nop 0
	v_mul_f32_e32 v82, v86, v82
	v_mul_f32_e32 v74, v86, v74
	v_mul_f32_e32 v82, v150, v82
	v_mul_f32_e32 v74, v151, v74
	v_cvt_pk_bf16_f32 v74, v82, v74
	v_mul_f32_e32 v82, v86, v83
	v_mul_f32_e32 v75, v86, v75
	v_mul_f32_e32 v82, v152, v82
	v_mul_f32_e32 v75, v153, v75
	v_cvt_pk_bf16_f32 v75, v82, v75
	v_mul_f32_e32 v82, v86, v84
	v_mul_f32_e32 v76, v86, v76
	v_mul_f32_e32 v82, v146, v82
	v_mul_f32_e32 v76, v147, v76
	v_cvt_pk_bf16_f32 v76, v82, v76
	v_mul_f32_e32 v82, v86, v85
	v_mul_f32_e32 v77, v86, v77
	v_mul_f32_e32 v82, v148, v82
	v_mul_f32_e32 v77, v149, v77
	v_cvt_pk_bf16_f32 v77, v82, v77
	v_cvt_f32_fp8_e32 v82, v158
	v_cvt_f32_fp8_sdwa v78, v158 src0_sel:BYTE_1
	v_cvt_f32_fp8_sdwa v83, v158 src0_sel:BYTE_2
	v_cvt_f32_fp8_sdwa v79, v158 src0_sel:BYTE_3
	v_mul_f32_e32 v86, v78, v78
	v_mul_f32_e32 v87, v79, v79
	v_cvt_f32_fp8_e32 v84, v159
	v_cvt_f32_fp8_sdwa v80, v159 src0_sel:BYTE_1
	v_fmac_f32_e32 v86, v82, v82
	v_fmac_f32_e32 v87, v83, v83
	v_add_f32_e32 v86, v86, v87
	v_mul_f32_e32 v87, v80, v80
	v_cvt_f32_fp8_sdwa v85, v159 src0_sel:BYTE_2
	v_cvt_f32_fp8_sdwa v81, v159 src0_sel:BYTE_3
	v_fmac_f32_e32 v87, v84, v84
	v_add_f32_e32 v86, v86, v87
	v_mul_f32_e32 v87, v81, v81
	v_fmac_f32_e32 v87, v85, v85
	v_add_f32_e32 v86, v86, v87
	s_nop 1
	v_add_f32_dpp v86, v86, v86 quad_perm:[1,0,3,2] row_mask:0xf bank_mask:0xf
	s_nop 1
	v_add_f32_dpp v86, v86, v86 quad_perm:[2,3,0,1] row_mask:0xf bank_mask:0xf
	s_nop 1
	v_add_f32_dpp v86, v86, v86 row_half_mirror row_mask:0xf bank_mask:0xf
	s_nop 1
	s_waitcnt lgkmcnt(0)
	v_add_f32_dpp v86, v86, v86 row_mirror row_mask:0xf bank_mask:0xf
	v_fmamk_f32 v86, v86, 0x3c000000, v167
	v_rsq_f32_e32 v86, v86
	s_nop 0
	v_mul_f32_e32 v82, v86, v82
	v_mul_f32_e32 v78, v86, v78
	v_mul_f32_e32 v82, v150, v82
	v_mul_f32_e32 v78, v151, v78
	v_cvt_pk_bf16_f32 v78, v82, v78
	v_mul_f32_e32 v82, v86, v83
	v_mul_f32_e32 v79, v86, v79
	v_mul_f32_e32 v82, v152, v82
	v_mul_f32_e32 v79, v153, v79
	v_cvt_pk_bf16_f32 v79, v82, v79
	v_mul_f32_e32 v82, v86, v84
	v_mul_f32_e32 v80, v86, v80
	v_mul_f32_e32 v82, v146, v82
	v_mul_f32_e32 v80, v147, v80
	v_cvt_pk_bf16_f32 v80, v82, v80
	v_mul_f32_e32 v82, v86, v85
	v_mul_f32_e32 v81, v86, v81
	v_mul_f32_e32 v82, v148, v82
	v_mul_f32_e32 v81, v149, v81
	v_cvt_pk_bf16_f32 v81, v82, v81
	v_add_u32_e32 v82, s1, v180
	ds_write_b128 v82, v[66:69]
	v_add_u32_e32 v66, s1, v181
	ds_write_b128 v66, v[70:73]
	v_add_u32_e32 v66, s1, v196
	ds_write_b128 v66, v[74:77] offset:32768
	v_add_u32_e32 v66, s1, v198
	ds_write_b128 v66, v[78:81] offset:32768
	v_mov_b32_e32 v0, v200
	s_waitcnt lgkmcnt(0)
	s_barrier
	s_cbranch_scc1 .LBB0_603
	s_branch .LBB0_469
